# fixup: f64 score dot products as straight-line code with prefetched LDS reads and two accumulation chains
# speedup vs baseline: 1.0354x; 1.0020x over previous
.LBB2_14:
	s_or_b64 exec, exec, s[0:1]
	s_waitcnt lgkmcnt(0)
	s_barrier
	s_and_saveexec_b64 s[0:1], s[18:19]
	s_cbranch_execz .LBB2_18
	v_mov_b64_e32 v[2:3], 0
	v_mov_b64_e32 v[72:73], 0
	v_mul_u32_u24_e32 v4, 0x210, v118
	s_waitcnt vmcnt(0)
	ds_read_b128 v[8:11], v132 offset:0
	ds_read_b128 v[12:15], v132 offset:16
	ds_read_b128 v[16:19], v4 offset:0
	ds_read_b128 v[20:23], v4 offset:16
	ds_read_b128 v[24:27], v132 offset:32
	ds_read_b128 v[28:31], v132 offset:48
	ds_read_b128 v[32:35], v4 offset:32
	ds_read_b128 v[36:39], v4 offset:48
	ds_read_b128 v[40:43], v132 offset:64
	ds_read_b128 v[44:47], v132 offset:80
	ds_read_b128 v[48:51], v4 offset:64
	ds_read_b128 v[52:55], v4 offset:80
	s_waitcnt lgkmcnt(8)
	v_cvt_f64_f32_e32 v[56:57], v8
	v_cvt_f64_f32_e32 v[58:59], v16
	v_fmac_f64_e32 v[2:3], v[56:57], v[58:59]
	v_cvt_f64_f32_e32 v[60:61], v9
	v_cvt_f64_f32_e32 v[62:63], v17
	v_fmac_f64_e32 v[72:73], v[60:61], v[62:63]
	v_cvt_f64_f32_e32 v[64:65], v10
	v_cvt_f64_f32_e32 v[66:67], v18
	v_fmac_f64_e32 v[2:3], v[64:65], v[66:67]
	v_cvt_f64_f32_e32 v[68:69], v11
	v_cvt_f64_f32_e32 v[70:71], v19
	v_fmac_f64_e32 v[72:73], v[68:69], v[70:71]
	v_cvt_f64_f32_e32 v[56:57], v12
	v_cvt_f64_f32_e32 v[58:59], v20
	v_fmac_f64_e32 v[2:3], v[56:57], v[58:59]
	v_cvt_f64_f32_e32 v[60:61], v13
	v_cvt_f64_f32_e32 v[62:63], v21
	v_fmac_f64_e32 v[72:73], v[60:61], v[62:63]
	v_cvt_f64_f32_e32 v[64:65], v14
	v_cvt_f64_f32_e32 v[66:67], v22
	v_fmac_f64_e32 v[2:3], v[64:65], v[66:67]
	v_cvt_f64_f32_e32 v[68:69], v15
	v_cvt_f64_f32_e32 v[70:71], v23
	v_fmac_f64_e32 v[72:73], v[68:69], v[70:71]
	ds_read_b128 v[8:11], v132 offset:96
	ds_read_b128 v[12:15], v132 offset:112
	ds_read_b128 v[16:19], v4 offset:96
	ds_read_b128 v[20:23], v4 offset:112
	s_waitcnt lgkmcnt(8)
	v_cvt_f64_f32_e32 v[56:57], v24
	v_cvt_f64_f32_e32 v[58:59], v32
	v_fmac_f64_e32 v[2:3], v[56:57], v[58:59]
	v_cvt_f64_f32_e32 v[60:61], v25
	v_cvt_f64_f32_e32 v[62:63], v33
	v_fmac_f64_e32 v[72:73], v[60:61], v[62:63]
	v_cvt_f64_f32_e32 v[64:65], v26
	v_cvt_f64_f32_e32 v[66:67], v34
	v_fmac_f64_e32 v[2:3], v[64:65], v[66:67]
	v_cvt_f64_f32_e32 v[68:69], v27
	v_cvt_f64_f32_e32 v[70:71], v35
	v_fmac_f64_e32 v[72:73], v[68:69], v[70:71]
	v_cvt_f64_f32_e32 v[56:57], v28
	v_cvt_f64_f32_e32 v[58:59], v36
	v_fmac_f64_e32 v[2:3], v[56:57], v[58:59]
	v_cvt_f64_f32_e32 v[60:61], v29
	v_cvt_f64_f32_e32 v[62:63], v37
	v_fmac_f64_e32 v[72:73], v[60:61], v[62:63]
	v_cvt_f64_f32_e32 v[64:65], v30
	v_cvt_f64_f32_e32 v[66:67], v38
	v_fmac_f64_e32 v[2:3], v[64:65], v[66:67]
	v_cvt_f64_f32_e32 v[68:69], v31
	v_cvt_f64_f32_e32 v[70:71], v39
	v_fmac_f64_e32 v[72:73], v[68:69], v[70:71]
	ds_read_b128 v[24:27], v132 offset:128
	ds_read_b128 v[28:31], v132 offset:144
	ds_read_b128 v[32:35], v4 offset:128
	ds_read_b128 v[36:39], v4 offset:144
	s_waitcnt lgkmcnt(8)
	v_cvt_f64_f32_e32 v[56:57], v40
	v_cvt_f64_f32_e32 v[58:59], v48
	v_fmac_f64_e32 v[2:3], v[56:57], v[58:59]
	v_cvt_f64_f32_e32 v[60:61], v41
	v_cvt_f64_f32_e32 v[62:63], v49
	v_fmac_f64_e32 v[72:73], v[60:61], v[62:63]
	v_cvt_f64_f32_e32 v[64:65], v42
	v_cvt_f64_f32_e32 v[66:67], v50
	v_fmac_f64_e32 v[2:3], v[64:65], v[66:67]
	v_cvt_f64_f32_e32 v[68:69], v43
	v_cvt_f64_f32_e32 v[70:71], v51
	v_fmac_f64_e32 v[72:73], v[68:69], v[70:71]
	v_cvt_f64_f32_e32 v[56:57], v44
	v_cvt_f64_f32_e32 v[58:59], v52
	v_fmac_f64_e32 v[2:3], v[56:57], v[58:59]
	v_cvt_f64_f32_e32 v[60:61], v45
	v_cvt_f64_f32_e32 v[62:63], v53
	v_fmac_f64_e32 v[72:73], v[60:61], v[62:63]
	v_cvt_f64_f32_e32 v[64:65], v46
	v_cvt_f64_f32_e32 v[66:67], v54
	v_fmac_f64_e32 v[2:3], v[64:65], v[66:67]
	v_cvt_f64_f32_e32 v[68:69], v47
	v_cvt_f64_f32_e32 v[70:71], v55
	v_fmac_f64_e32 v[72:73], v[68:69], v[70:71]
	ds_read_b128 v[40:43], v132 offset:160
	ds_read_b128 v[44:47], v132 offset:176
	ds_read_b128 v[48:51], v4 offset:160
	ds_read_b128 v[52:55], v4 offset:176
	s_waitcnt lgkmcnt(8)
	v_cvt_f64_f32_e32 v[56:57], v8
	v_cvt_f64_f32_e32 v[58:59], v16
	v_fmac_f64_e32 v[2:3], v[56:57], v[58:59]
	v_cvt_f64_f32_e32 v[60:61], v9
	v_cvt_f64_f32_e32 v[62:63], v17
	v_fmac_f64_e32 v[72:73], v[60:61], v[62:63]
	v_cvt_f64_f32_e32 v[64:65], v10
	v_cvt_f64_f32_e32 v[66:67], v18
	v_fmac_f64_e32 v[2:3], v[64:65], v[66:67]
	v_cvt_f64_f32_e32 v[68:69], v11
	v_cvt_f64_f32_e32 v[70:71], v19
	v_fmac_f64_e32 v[72:73], v[68:69], v[70:71]
	v_cvt_f64_f32_e32 v[56:57], v12
	v_cvt_f64_f32_e32 v[58:59], v20
	v_fmac_f64_e32 v[2:3], v[56:57], v[58:59]
	v_cvt_f64_f32_e32 v[60:61], v13
	v_cvt_f64_f32_e32 v[62:63], v21
	v_fmac_f64_e32 v[72:73], v[60:61], v[62:63]
	v_cvt_f64_f32_e32 v[64:65], v14
	v_cvt_f64_f32_e32 v[66:67], v22
	v_fmac_f64_e32 v[2:3], v[64:65], v[66:67]
	v_cvt_f64_f32_e32 v[68:69], v15
	v_cvt_f64_f32_e32 v[70:71], v23
	v_fmac_f64_e32 v[72:73], v[68:69], v[70:71]
	ds_read_b128 v[8:11], v132 offset:192
	ds_read_b128 v[12:15], v132 offset:208
	ds_read_b128 v[16:19], v4 offset:192
	ds_read_b128 v[20:23], v4 offset:208
	s_waitcnt lgkmcnt(8)
	v_cvt_f64_f32_e32 v[56:57], v24
	v_cvt_f64_f32_e32 v[58:59], v32
	v_fmac_f64_e32 v[2:3], v[56:57], v[58:59]
	v_cvt_f64_f32_e32 v[60:61], v25
	v_cvt_f64_f32_e32 v[62:63], v33
	v_fmac_f64_e32 v[72:73], v[60:61], v[62:63]
	v_cvt_f64_f32_e32 v[64:65], v26
	v_cvt_f64_f32_e32 v[66:67], v34
	v_fmac_f64_e32 v[2:3], v[64:65], v[66:67]
	v_cvt_f64_f32_e32 v[68:69], v27
	v_cvt_f64_f32_e32 v[70:71], v35
	v_fmac_f64_e32 v[72:73], v[68:69], v[70:71]
	v_cvt_f64_f32_e32 v[56:57], v28
	v_cvt_f64_f32_e32 v[58:59], v36
	v_fmac_f64_e32 v[2:3], v[56:57], v[58:59]
	v_cvt_f64_f32_e32 v[60:61], v29
	v_cvt_f64_f32_e32 v[62:63], v37
	v_fmac_f64_e32 v[72:73], v[60:61], v[62:63]
	v_cvt_f64_f32_e32 v[64:65], v30
	v_cvt_f64_f32_e32 v[66:67], v38
	v_fmac_f64_e32 v[2:3], v[64:65], v[66:67]
	v_cvt_f64_f32_e32 v[68:69], v31
	v_cvt_f64_f32_e32 v[70:71], v39
	v_fmac_f64_e32 v[72:73], v[68:69], v[70:71]
	ds_read_b128 v[24:27], v132 offset:224
	ds_read_b128 v[28:31], v132 offset:240
	ds_read_b128 v[32:35], v4 offset:224
	ds_read_b128 v[36:39], v4 offset:240
	s_waitcnt lgkmcnt(8)
	v_cvt_f64_f32_e32 v[56:57], v40
	v_cvt_f64_f32_e32 v[58:59], v48
	v_fmac_f64_e32 v[2:3], v[56:57], v[58:59]
	v_cvt_f64_f32_e32 v[60:61], v41
	v_cvt_f64_f32_e32 v[62:63], v49
	v_fmac_f64_e32 v[72:73], v[60:61], v[62:63]
	v_cvt_f64_f32_e32 v[64:65], v42
	v_cvt_f64_f32_e32 v[66:67], v50
	v_fmac_f64_e32 v[2:3], v[64:65], v[66:67]
	v_cvt_f64_f32_e32 v[68:69], v43
	v_cvt_f64_f32_e32 v[70:71], v51
	v_fmac_f64_e32 v[72:73], v[68:69], v[70:71]
	v_cvt_f64_f32_e32 v[56:57], v44
	v_cvt_f64_f32_e32 v[58:59], v52
	v_fmac_f64_e32 v[2:3], v[56:57], v[58:59]
	v_cvt_f64_f32_e32 v[60:61], v45
	v_cvt_f64_f32_e32 v[62:63], v53
	v_fmac_f64_e32 v[72:73], v[60:61], v[62:63]
	v_cvt_f64_f32_e32 v[64:65], v46
	v_cvt_f64_f32_e32 v[66:67], v54
	v_fmac_f64_e32 v[2:3], v[64:65], v[66:67]
	v_cvt_f64_f32_e32 v[68:69], v47
	v_cvt_f64_f32_e32 v[70:71], v55
	v_fmac_f64_e32 v[72:73], v[68:69], v[70:71]
	s_waitcnt lgkmcnt(4)
	v_cvt_f64_f32_e32 v[56:57], v8
	v_cvt_f64_f32_e32 v[58:59], v16
	v_fmac_f64_e32 v[2:3], v[56:57], v[58:59]
	v_cvt_f64_f32_e32 v[60:61], v9
	v_cvt_f64_f32_e32 v[62:63], v17
	v_fmac_f64_e32 v[72:73], v[60:61], v[62:63]
	v_cvt_f64_f32_e32 v[64:65], v10
	v_cvt_f64_f32_e32 v[66:67], v18
	v_fmac_f64_e32 v[2:3], v[64:65], v[66:67]
	v_cvt_f64_f32_e32 v[68:69], v11
	v_cvt_f64_f32_e32 v[70:71], v19
	v_fmac_f64_e32 v[72:73], v[68:69], v[70:71]
	v_cvt_f64_f32_e32 v[56:57], v12
	v_cvt_f64_f32_e32 v[58:59], v20
	v_fmac_f64_e32 v[2:3], v[56:57], v[58:59]
	v_cvt_f64_f32_e32 v[60:61], v13
	v_cvt_f64_f32_e32 v[62:63], v21
	v_fmac_f64_e32 v[72:73], v[60:61], v[62:63]
	v_cvt_f64_f32_e32 v[64:65], v14
	v_cvt_f64_f32_e32 v[66:67], v22
	v_fmac_f64_e32 v[2:3], v[64:65], v[66:67]
	v_cvt_f64_f32_e32 v[68:69], v15
	v_cvt_f64_f32_e32 v[70:71], v23
	v_fmac_f64_e32 v[72:73], v[68:69], v[70:71]
	s_waitcnt lgkmcnt(0)
	v_cvt_f64_f32_e32 v[56:57], v24
	v_cvt_f64_f32_e32 v[58:59], v32
	v_fmac_f64_e32 v[2:3], v[56:57], v[58:59]
	v_cvt_f64_f32_e32 v[60:61], v25
	v_cvt_f64_f32_e32 v[62:63], v33
	v_fmac_f64_e32 v[72:73], v[60:61], v[62:63]
	v_cvt_f64_f32_e32 v[64:65], v26
	v_cvt_f64_f32_e32 v[66:67], v34
	v_fmac_f64_e32 v[2:3], v[64:65], v[66:67]
	v_cvt_f64_f32_e32 v[68:69], v27
	v_cvt_f64_f32_e32 v[70:71], v35
	v_fmac_f64_e32 v[72:73], v[68:69], v[70:71]
	v_cvt_f64_f32_e32 v[56:57], v28
	v_cvt_f64_f32_e32 v[58:59], v36
	v_fmac_f64_e32 v[2:3], v[56:57], v[58:59]
	v_cvt_f64_f32_e32 v[60:61], v29
	v_cvt_f64_f32_e32 v[62:63], v37
	v_fmac_f64_e32 v[72:73], v[60:61], v[62:63]
	v_cvt_f64_f32_e32 v[64:65], v30
	v_cvt_f64_f32_e32 v[66:67], v38
	v_fmac_f64_e32 v[2:3], v[64:65], v[66:67]
	v_cvt_f64_f32_e32 v[68:69], v31
	v_cvt_f64_f32_e32 v[70:71], v39
	v_fmac_f64_e32 v[72:73], v[68:69], v[70:71]
	v_add_f64 v[2:3], v[2:3], v[72:73]
	v_ldexp_f64 v[2:3], v[2:3], -3
	ds_write_b64 v119, v[2:3]
